# phase 3: static mixer roles; 32 HGRN workgroups convert expert items 0..255 (four-deep shared loop) before their unit, the other 768 items after the mixers
# speedup vs baseline: 1.0102x; 1.0048x over previous
.LBB0_640:
	s_add_u32 s0, s96, 0x17400000
	s_addc_u32 s1, s97, 0
	s_add_u32 s82, s96, 0x7400000
	s_addc_u32 s83, s97, 0
	v_writelane_b32 v254, s0, 57
	s_cmp_lt_i32 s48, 4
	v_lshlrev_b32_e32 v253, 4, v0
	v_writelane_b32 v254, s1, 58
	s_cselect_b64 s[0:1], -1, 0
	s_cmp_gt_i32 s49, 3
	s_cselect_b64 s[2:3], -1, 0
	s_and_b64 s[0:1], s[0:1], s[2:3]
	s_andn2_b64 vcc, exec, s[0:1]
	v_lshlrev_b32_e32 v179, 3, v0
	v_mbcnt_lo_u32_b32 v252, -1, 0
	s_cbranch_vccnz .LBB0_974
	v_readlane_b32 s0, v254, 55
	s_and_b32 s0, s0, 7
	s_cmp_lg_u32 s0, 2
	s_cbranch_scc1 mkcq_p3mix
	s_mov_b32 s98, 2
	s_mov_b32 s99, 0
	s_movk_i32 s100, 0xff
	s_movk_i32 s101, 0x200
	v_lshlrev_b32_e32 v4, 2, v0
	s_branch mkcq_common
mkcq_p3mix:
	s_mov_b32 s98, 0
	v_and_b32_e32 v124, 0x7f, v0
	v_lshlrev_b32_e32 v11, 2, v124
	s_add_i32 s4, 0, 0x1c000
	v_readlane_b32 s5, v254, 44
	v_lshrrev_b32_e32 v165, 4, v1
	v_and_b32_e32 v5, 0xf0, v253
	s_add_i32 s0, 0, 0x1ca00
	v_lshlrev_b32_e32 v8, 1, v124
	v_add_u32_e32 v133, s4, v11
	s_lshr_b32 s10, s69, 7
	s_lshl_b32 s4, s5, 1
	v_and_b32_e32 v164, 15, v0
	v_lshrrev_b32_e32 v4, 4, v0
	v_add_u32_e32 v128, s0, v5
	v_add_u32_e32 v9, s0, v8
	s_add_i32 s0, 0, 0x1c200
	s_and_b32 s11, s4, 2
	s_lshl_b32 s4, s10, 4
	v_lshlrev_b32_e32 v130, 2, v165
	v_lshrrev_b32_e32 v3, 7, v0
	v_mul_u32_u24_e32 v2, 0x9000, v4
	v_lshrrev_b32_e32 v106, 3, v0
	s_add_i32 s3, 0, 0x13c00
	v_add_u32_e32 v132, s0, v11
	v_or_b32_e32 v11, s4, v130
	v_or_b32_e32 v12, s4, v164
	s_and_b32 s4, s69, 0xffffffc0
	v_or_b32_e32 v125, v2, v5
	v_mul_u32_u24_e32 v2, 0x9000, v106
	v_and_b32_e32 v108, 0x70, v253
	s_add_i32 s1, 0, 0x20a00
	v_lshlrev_b32_e32 v7, 12, v3
	s_lshl_b32 s33, s5, 5
	s_add_i32 s18, 0, 0x11800
	s_add_i32 s4, s4, s3
	v_mul_u32_u24_e32 v21, 0x1100, v3
	v_mul_u32_u24_e32 v22, 0x1200, v3
	v_lshl_or_b32 v3, v3, 4, 1
	v_lshl_or_b32 v2, v108, 1, v2
	s_movk_i32 s12, 0x110
	v_mov_b32_e32 v109, 0
	v_mul_u32_u24_e32 v23, 0x110, v3
	v_mul_u32_u24_e32 v24, 0x120, v3
	s_cmp_le_u32 s11, s10
	v_lshl_or_b32 v3, s11, 4, v164
	s_movk_i32 s13, 0x90
	v_or_b32_e32 v27, 1, v11
	v_or_b32_e32 v28, 2, v11
	v_or_b32_e32 v29, 3, v11
	v_or_b32_e32 v31, 16, v164
	v_readlane_b32 s40, v254, 23
	v_bfe_u32 v107, v0, 2, 2
	v_add_u32_e32 v127, 0x6000, v2
	v_lshlrev_b32_e32 v2, 2, v108
	v_mul_lo_u32 v12, v12, s12
	v_lshlrev_b32_e32 v135, 3, v165
	v_mad_u32_u24 v137, v164, s12, 0
	v_or_b32_e32 v20, 0x200, v0
	s_cselect_b64 s[34:35], -1, 0
	v_mul_u32_u24_e32 v25, 0x110, v3
	v_mul_lo_u32 v26, v11, s13
	s_cmp_lt_u32 s11, s10
	v_or_b32_e32 v30, 16, v3
	v_mad_u32_u24 v142, v31, s12, 0
	v_lshl_add_u32 v32, v3, 1, s18
	v_cmp_gt_u32_e64 s[10:11], v3, v11
	v_cmp_gt_u32_e64 s[12:13], v3, v27
	v_cmp_gt_u32_e64 s[14:15], v3, v28
	v_cmp_gt_u32_e64 s[16:17], v3, v29
	v_mov_b32_e32 v3, v109
	v_readlane_b32 s44, v254, 27
	v_readlane_b32 s45, v254, 28
	v_add_u32_e32 v6, s3, v2
	v_and_b32_e32 v13, 48, v0
	v_or_b32_e32 v14, v135, v107
	v_and_b32_e32 v136, 24, v179
	v_or_b32_e32 v17, 16, v130
	s_movk_i32 s3, 0x120
	v_lshrrev_b32_e32 v20, 4, v20
	v_lshl_add_u64 v[110:111], s[44:45], 0, v[2:3]
	v_lshl_add_u64 v[2:3], s[96:97], 0, v[108:109]
	s_mov_b64 s[26:27], 0x3400000
	v_lshl_or_b32 v108, v106, 11, v108
	v_add_u32_e32 v129, s1, v5
	v_add_u32_e32 v5, 0, v5
	v_add_u32_e32 v10, s1, v8
	v_add_u32_e32 v8, 0, v8
	s_movk_i32 s2, 0x80
	v_add_u32_e32 v12, 0, v12
	v_add_u32_e32 v134, 0, v13
	v_or_b32_e32 v15, s33, v136
	v_add_u32_e32 v16, s18, v13
	s_waitcnt vmcnt(1)
	v_lshl_add_u32 v18, v164, 2, s4
	s_waitcnt vmcnt(0)
	v_mul_u32_u24_e32 v19, 0x210, v106
	v_lshlrev_b32_e32 v138, 8, v4
	v_mul_u32_u24_e32 v4, 0x120, v4
	v_lshlrev_b32_e32 v139, 8, v20
	v_mul_u32_u24_e32 v20, 0x120, v20
	s_movk_i32 s4, 0xff
	s_movk_i32 s6, 0x17f
	s_movk_i32 s8, 0x1ff
	v_mad_u32_u24 v140, v14, s3, 0
	v_mul_u32_u24_e32 v14, 0x90, v164
	v_lshlrev_b32_e32 v141, 1, v17
	v_mul_u32_u24_e32 v31, 0x840, v165
	v_mul_u32_u24_e32 v17, 0x210, v17
	v_lshl_add_u32 v33, v30, 1, s18
	v_readlane_b32 s42, v254, 25
	v_readlane_b32 s43, v254, 26
	v_readlane_b32 s46, v254, 29
	v_readlane_b32 s47, v254, 30
	v_readlane_b32 s48, v254, 31
	v_lshl_add_u64 v[112:113], v[2:3], 0, s[26:27]
	v_lshl_add_u64 v[2:3], s[96:97], 0, v[108:109]
	s_mov_b64 s[26:27], 0x33e0000
	v_add_u32_e32 v126, 0x120000, v125
	s_mov_b32 s31, 0
	v_lshl_add_u32 v131, v0, 2, s0
	v_cmp_gt_u32_e64 s[0:1], s2, v0
	v_cmp_lt_u32_e64 s[4:5], s4, v0
	v_cmp_lt_u32_e64 s[6:7], s6, v0
	v_cmp_lt_u32_e64 s[8:9], s8, v0
	s_cselect_b64 s[36:37], -1, 0
	v_add_u32_e32 v143, 0x1100, v142
	v_add_u32_e32 v144, 0x2200, v142
	v_or_b32_e32 v145, 64, v135
	v_or_b32_e32 v146, 0x60, v135
	v_cmp_gt_u32_e64 s[18:19], v30, v11
	v_cmp_gt_u32_e64 s[20:21], v30, v27
	v_cmp_gt_u32_e64 s[22:23], v30, v28
	v_cmp_gt_u32_e64 s[24:25], v30, v29
	v_lshl_add_u64 v[114:115], v[2:3], 0, s[26:27]
	s_add_i32 s3, 0, 0x26400
	s_movk_i32 s42, 0x4000
	s_movk_i32 s43, 0x3000
	s_movk_i32 s44, 0x5000
	v_add_u32_e32 v147, v5, v4
	v_add_u32_e32 v148, v5, v20
	v_add_u32_e32 v149, v9, v7
	v_add_u32_e32 v150, v10, v7
	s_mov_b32 s45, 0x800000
	s_mov_b32 s46, 0x3f317217
	s_mov_b32 s47, 0x7f800000
	s_movk_i32 s48, 0x7fff
	v_add_u32_e32 v151, v8, v21
	v_add_u32_e32 v152, v8, v22
	v_add_u32_e32 v153, v8, v23
	v_add_u32_e32 v154, v8, v24
	v_add_u32_e32 v155, v32, v26
	v_add_u32_e32 v156, v33, v26
	v_add_u32_e32 v157, v140, v15
	v_add_u32_e32 v158, v16, v14
	v_add_u32_e32 v159, v18, v31
	v_add_u32_e32 v160, v18, v17
	v_add_u32_e32 v161, v6, v19
	v_mov_b32_e32 v162, 0x358637bd
	v_mov_b32_e32 v163, 0x41b17218
	v_add_u32_e32 v167, v12, v13
	v_add_u32_e32 v168, v134, v25
	v_mbcnt_hi_u32_b32 v166, -1, v252
	v_readlane_b32 s41, v254, 24
	v_readlane_b32 s49, v254, 32
	v_readlane_b32 s50, v254, 33
	v_readlane_b32 s51, v254, 34
	v_readlane_b32 s52, v254, 35
	v_readlane_b32 s53, v254, 36
	v_readlane_b32 s54, v254, 37
	v_readlane_b32 s55, v254, 38
	s_branch .LBB0_644

.LBB0_644:
	v_readlane_b32 s26, v254, 55
	s_bitcmp1_b32 s26, 0
	s_cbranch_scc1 .LBB0_668
	s_barrier
	s_mov_b64 s[26:27], exec
	v_readlane_b32 s28, v254, 5
	v_readlane_b32 s29, v254, 6
	s_and_b64 s[28:29], s[26:27], s[28:29]
	s_mov_b64 exec, s[28:29]
	s_cbranch_execz .LBB0_648
	s_mov_b64 s[40:41], exec
	v_mbcnt_lo_u32_b32 v2, s40, 0
	v_mbcnt_hi_u32_b32 v2, s41, v2
	v_cmp_eq_u32_e32 vcc, 0, v2
	s_and_saveexec_b64 s[38:39], vcc
	s_cbranch_execz .LBB0_647
	s_bcnt1_i32_b64 s28, s[40:41]
	v_mov_b32_e32 v3, s28
	global_atomic_add v3, v109, v3, s[96:97] offset:256 sc0

.LBB0_893:
	v_readlane_b32 s3, v254, 44
	s_lshl_b32 s0, s3, 14
	s_lshl_b32 s2, s3, 3
	s_lshl_b32 s3, s3, 8
	s_and_b32 s4, s3, 0x700
	s_add_i32 s0, s0, 0
	s_lshl_b32 s5, s4, 10
	v_readlane_b32 s6, v254, 57
	v_readlane_b32 s7, v254, 58
	s_add_u32 s5, s6, s5
	v_lshrrev_b32_e32 v66, 3, v1
	s_waitcnt vmcnt(14)
	v_and_b32_e32 v2, 28, v167
	v_and_b32_e32 v76, 56, v179
	s_addc_u32 s20, s7, 0
	v_mov_b32_e32 v69, 0
	v_lshl_add_u32 v3, v2, 2, s0
	v_mul_u32_u24_e32 v4, 0x84, v66
	v_mul_u32_u24_e32 v5, 0x84, v76
	s_waitcnt vmcnt(4)
	v_lshlrev_b32_e32 v6, 2, v66
	s_add_i32 s21, 0, 0x26600
	v_readlane_b32 s76, v254, 49
	s_mov_b32 s1, 0
	v_or_b32_e32 v70, 8, v66
	v_or_b32_e32 v72, 16, v66
	v_or_b32_e32 v74, 24, v66
	v_or_b32_e32 v67, 32, v66
	v_or_b32_e32 v71, 40, v66
	v_or_b32_e32 v73, 48, v66
	v_or_b32_e32 v75, 56, v66
	v_mov_b32_e32 v77, v69
	v_add3_u32 v78, s0, v5, v6
	v_mov_b32_e32 v79, s21
	s_movk_i32 s22, 0x3ff
	s_lshl_b32 s23, s4, 2
	s_mov_b32 s4, 0x42000000
	v_lshlrev_b32_e32 v68, 2, v2
	v_add_u32_e32 v80, v3, v4
	v_readlane_b32 s77, v254, 50
	v_readlane_b32 s78, v254, 51
	v_readlane_b32 s79, v254, 52
	v_readlane_b32 s72, v255, 9
	v_readlane_b32 s81, v255, 8
	v_readlane_b32 s69, v254, 59
	v_readlane_b32 s73, v254, 55
	v_readlane_b32 s80, v254, 56
	v_lshlrev_b32_e32 v4, 2, v0
	s_mov_b32 s98, 1
	s_movk_i32 s99, 0x100
	s_movk_i32 s100, 0x3ff
	s_mov_b32 s101, 0
	s_branch mkcq_common

.LBB0_1334:
	s_cmp_eq_u32 s98, 1
	s_cbranch_scc1 mkcq_p3ret
	s_cmp_eq_u32 s98, 2
	s_cbranch_scc1 mkcq_p3mix
	v_readlane_b32 s48, v254, 53
	v_readlane_b32 s49, v254, 54
	s_cmp_lt_i32 s49, 9
	s_barrier
	s_cbranch_scc1 .LBB0_1388
	s_waitcnt vmcnt(0)
	s_barrier
	s_mov_b64 s[0:1], exec
	v_readlane_b32 s2, v254, 5
	v_readlane_b32 s3, v254, 6
	s_and_b64 s[2:3], s[0:1], s[2:3]
	s_mov_b64 exec, s[2:3]
	s_cbranch_execz .LBB0_1387
	s_add_i32 s2, 0, 0x26160
	v_mov_b32_e32 v2, s2
	s_waitcnt vmcnt(0) expcnt(0) lgkmcnt(0)
	ds_read_b32 v4, v2
	s_add_i32 s2, 0, 0x26164
	v_mov_b32_e32 v2, s2
	ds_read_b32 v2, v2
	s_waitcnt lgkmcnt(1)
	v_cmp_ne_u32_e32 vcc, 0, v4
	s_cbranch_vccnz .LBB0_1351
	v_readlane_b32 s2, v254, 0
	v_readlane_b32 s3, v254, 1
	s_load_dwordx2 s[6:7], s[2:3], 0x4
	s_add_u32 s2, s96, 0x4200
	s_addc_u32 s3, s97, 0
	s_add_u32 s4, s96, 0x4400
	s_addc_u32 s5, s97, 0
	s_waitcnt lgkmcnt(0)
	s_mul_i32 s33, s6, s72
	s_add_u32 s6, s96, 0x4500
	s_mul_i32 s33, s33, s7
	s_addc_u32 s7, s97, 0
	s_add_u32 s8, s96, 0x4600
	s_addc_u32 s9, s97, 0
	s_add_u32 s10, s96, 0x4700
	s_addc_u32 s11, s97, 0
	s_add_u32 s18, s96, 0x4800
	s_addc_u32 s19, s97, 0
	s_add_u32 s20, s96, 0x4900
	s_addc_u32 s21, s97, 0
	s_add_u32 s22, s96, 0x4a00
	s_addc_u32 s23, s97, 0
	s_add_u32 s24, s96, 0x4b00
	s_addc_u32 s25, s97, 0
	s_add_u32 s26, s96, 0x4c00
	s_addc_u32 s27, s97, 0
	s_add_u32 s28, s96, 0x4d00
	s_addc_u32 s29, s97, 0
	s_add_u32 s30, s96, 0x4e00
	s_addc_u32 s31, s97, 0
	s_add_u32 s34, s96, 0x4f00
	s_addc_u32 s35, s97, 0
	s_add_u32 s36, s96, 0x5000
	s_addc_u32 s37, s97, 0
	s_add_u32 s38, s96, 0x5100
	s_addc_u32 s39, s97, 0
	s_add_u32 s40, s96, 0x5200
	s_addc_u32 s41, s97, 0
	s_add_u32 s42, s96, 0x5300
	s_addc_u32 s43, s97, 0
	s_mov_b32 s50, 1
	v_mov_b32_e32 v18, 0
	s_branch .LBB0_1339
